# W1 weight conversion: workgroups with blockIdx bit3 set run their share before the tail phase instead of after it, so half the chip streams weights while the other half runs the latency-bound tail
# speedup vs baseline: 1.0136x; 1.0107x over previous
; #define LAS __attribute__((address_space(3)))
; #define REP(n) for (int rep_ = 0; rep_ < 1 + ((REPMASK >> (n)) & 1); ++rep_)
; #define IN(k) (lo <= (k) && (k) < hi && ((F = make_frame((LAS unsigned char*)lds_raw, wv)), true))
; #define SEAM(k) do { if ((k) + 1 < hi) xcd_barrier(bar, tid_now(wv) == 0); } while (0)
; DI void phase_expert_weights(const Frame& F, int l, int which) {
;     LAS float* scr = (LAS float*)(F.lds + F.wave * 16384);
;     unsigned char* ws = F.ws;
;     if (which == 0) {
;         constexpr int IPM = (D / 64) * (2048 / 32);
;         for (int it = F.gw; it < NE * IPM; it += F.NGW) { const int mtx = l * NE + it / IPM, r = it % IPM;
;             transpose_item(F.ap->in[32] + (size_t)mtx * D * 2048, D, 2048, (bf16_t*)(ws + WS_W1 + (size_t)mtx * 2048 * D), 3, scr, r, F.lane); }
; __global__ void __launch_bounds__(NTHR, 2) fwd_kernel(Args args) {
;     ...
;         REP(11) if (PM(11)) if (IN(pb + 8)) { phase_tail(F, l); SEAM(pb + 8); }
;         if (IN(pb + 9)) { phase_expert_weights(F, l, 0); SEAM(pb + 9); }
.LBB0_951:
	v_readlane_b32 s8, v253, 56
	v_readlane_b32 s9, v253, 57
	s_cmp_gt_i32 s96, s17
	s_mov_b32 s9, s29
	s_cselect_b64 s[4:5], -1, 0
	s_lshl_b32 s28, s8, 5
	v_writelane_b32 v253, s8, 56
	s_xor_b64 s[6:7], s[38:39], -1
	s_lshl_b64 s[48:49], s[8:9], 3
	v_writelane_b32 v253, s9, 57
	s_nop 0
	v_readlane_b32 s2, v253, 58
	s_or_b32 s17, s2, 11
	s_cmp_lt_i32 s17, s97
	s_cselect_b64 s[50:51], -1, 0
	s_or_b64 s[4:5], s[4:5], s[6:7]
	s_and_b64 vcc, exec, s[4:5]
	s_cbranch_vccnz .LBB0_1102
	s_bitcmp0_b32 s94, 3
	s_cbranch_scc1 .Lpre_skip
	s_mov_b32 s22, s10
	s_mov_b32 s23, s17
	s_mov_b64 s[24:25], s[38:39]
	v_mov_b32_e32 v42, v17
	s_mov_b64 s[4:5], s[58:59]
	v_readlane_b32 s2, v252, 0
	s_waitcnt lgkmcnt(0)
	v_mbcnt_lo_u32_b32 v0, -1, 0
	v_mbcnt_hi_u32_b32 v0, -1, v0
	s_mov_b32 s6, s94
	v_add_u32_e32 v1, s2, v0
	s_mov_b32 s2, s60
	s_and_b32 s7, s2, 7
	s_cmp_lg_u32 s7, 0
	v_readfirstlane_b32 s7, v1
	s_cbranch_scc1 .Lpre_1107
	s_ashr_i32 s9, s6, 31
	s_lshr_b32 s9, s9, 29
	s_add_i32 s9, s6, s9
	s_ashr_i32 s10, s9, 3
	s_and_b32 s9, s9, -8
	s_ashr_i32 s8, s2, 3
	s_sub_i32 s6, s6, s9
	s_mul_i32 s6, s8, s6
	s_add_i32 s6, s6, s10

; #define LAS __attribute__((address_space(3)))
; DI float kf(float c) { asm volatile("" : "+v"(c)); return c; }
; DI unsigned pk2(float lo, float hi) { return f2bf(lo) | (f2bf(hi) << 16); }
; DI void phase_tail(const Frame& F, int l) {
;     const float* MOD = (const float*)(F.ws + WS_MOD);
;     LAS bf16_t* Ht = (LAS bf16_t*)F.lds;
;     LAS float* Pz = (LAS float*)(F.lds + TL_PZ);
;     LAS unsigned* hist = (LAS unsigned*)(F.lds + L_HIST);
;     LAS unsigned* basew = (LAS unsigned*)(F.lds + L_BASE);
;     const int r = F.lane & 31, h = F.lane >> 5;
;     bf16x8 RWf[8];
;     { const float* rw = (const float*)(F.ws + WS_RWT) + ((size_t)l * 32 + r) * D + 128 * F.wave + 8 * h;
; #pragma unroll
;       for (int s = 0; s < 8; ++s) { const f32x4 a = *(const f32x4*)(rw + 16 * s), b = *(const f32x4*)(rw + 16 * s + 4);
;           u32x4 p; p.x = pk2(a.x, a.y); p.y = pk2(a.z, a.w); p.z = pk2(b.x, b.y); p.w = pk2(b.z, b.w); RWf[s] = __builtin_bit_cast(bf16x8, p); } }
;     if (F.tid < 32) hist[F.tid] = 0u;
;     __syncthreads();
;     int* tok_e = (int*)(F.ws + WS_TOKE); int* tok_p = (int*)(F.ws + WS_TOKP); float* tok_g = (float*)(F.ws + WS_TOKG);
;     const float rb = F.ap->in[31][l * 32 + r]; const float neg_big = kf(-3.0e38f);
;     for (int ti = F.vcu; ti < T / 32; ti += F.G) {
.Lpre_done:
	s_mov_b32 s10, s22
	s_mov_b32 s17, s23
	s_mov_b64 s[38:39], s[24:25]
	v_mov_b32_e32 v17, v42
.Lpre_skip:
	s_mov_b64 s[40:41], s[58:59]
	v_readlane_b32 s2, v252, 0
	s_mov_b32 s52, s94
	s_mov_b32 s8, s60
	v_mbcnt_lo_u32_b32 v16, -1, 0
	v_mbcnt_hi_u32_b32 v16, -1, v16
	s_waitcnt lgkmcnt(0)
	v_add_u32_e32 v66, s2, v16
	s_and_b32 s2, s8, 7
	s_cmp_lg_u32 s2, 0
	v_readfirstlane_b32 s2, v66
	s_cbranch_scc1 .LBB0_954
	s_ashr_i32 s5, s52, 31
	s_lshr_b32 s5, s5, 29
	s_add_i32 s5, s52, s5
	s_ashr_i32 s6, s5, 3
	s_and_b32 s5, s5, -8
	s_ashr_i32 s4, s8, 3
	s_sub_i32 s5, s52, s5
	s_mul_i32 s4, s4, s5
	s_add_i32 s52, s4, s6

; #define LAS __attribute__((address_space(3)))
; #define IN(k) (lo <= (k) && (k) < hi && ((F = make_frame((LAS unsigned char*)lds_raw, wv)), true))
; #define SEAM(k) do { if ((k) + 1 < hi) xcd_barrier(bar, tid_now(wv) == 0); } while (0)
; DI void phase_expert_weights(const Frame& F, int l, int which) {
;     LAS float* scr = (LAS float*)(F.lds + F.wave * 16384);
;     unsigned char* ws = F.ws;
;     if (which == 0) {
;         constexpr int IPM = (D / 64) * (2048 / 32);
;         for (int it = F.gw; it < NE * IPM; it += F.NGW) { const int mtx = l * NE + it / IPM, r = it % IPM;
;             transpose_item(F.ap->in[32] + (size_t)mtx * D * 2048, D, 2048, (bf16_t*)(ws + WS_W1 + (size_t)mtx * 2048 * D), 3, scr, r, F.lane); }
; __global__ void __launch_bounds__(NTHR, 2) fwd_kernel(Args args) {
;     ...
;         if (IN(pb + 9)) { phase_expert_weights(F, l, 0); SEAM(pb + 9); }
.LBB0_1104:
	v_readlane_b32 s50, v253, 50
	s_andn2_b64 vcc, exec, s[4:5]
	v_readlane_b32 s51, v253, 51
	s_cbranch_vccnz .LBB0_1160
	s_bitcmp1_b32 s94, 3
	s_cbranch_scc1 .LBB0_1110
	s_mov_b64 s[4:5], s[58:59]
	v_readlane_b32 s2, v252, 0
	s_waitcnt lgkmcnt(0)
	v_mbcnt_lo_u32_b32 v0, -1, 0
	v_mbcnt_hi_u32_b32 v0, -1, v0
	s_mov_b32 s6, s94
	v_add_u32_e32 v1, s2, v0
	s_mov_b32 s2, s60
	s_and_b32 s7, s2, 7
	s_cmp_lg_u32 s7, 0
	v_readfirstlane_b32 s7, v1
	s_cbranch_scc1 .LBB0_1107
	s_ashr_i32 s9, s6, 31
	s_lshr_b32 s9, s9, 29
	s_add_i32 s9, s6, s9
	s_ashr_i32 s10, s9, 3
	s_and_b32 s9, s9, -8
	s_ashr_i32 s8, s2, 3
	s_sub_i32 s6, s6, s9
	s_mul_i32 s6, s8, s6
	s_add_i32 s6, s6, s10
